# cmp pass 1 copy removal with the two loop-carried copies placed first so the score MFMA results keep their 12-state distance to the max chain
# baseline (speedup 1.0000x reference)
; __device__ __forceinline__ float xmax16(float v) { float a = v, b = v; PL_SWAP16(a, b); return fmaxf(a, b); }
; __device__ __forceinline__ float xmax32(float v) { float a = v, b = v; PL_SWAP32(a, b); return fmaxf(a, b); }
; template <bool WITH_O, class G> __device__ __forceinline__ void online_smc(f32x4 (&s)[4], G& g, const float ref) {
;     float mx = s[0][0];
; #pragma unroll
;     for (int T_ = 0; T_ < 4; ++T_)
; #pragma unroll
;         for (int i = 0; i < 4; ++i) mx = fmaxf(mx, s[T_][i]);
;     const float t = mx + ref;
;     if (!__all(t <= g.m + SM_THR)) {
;         const float mr = xmax32(xmax16(t));
;         const float mn = fmaxf(g.m, mr); const float al = __builtin_amdgcn_exp2f(g.m - mn); g.m = mn; g.l *= al;
.LBB0_1579:
	s_mov_b64 s[22:23], -1
	s_and_b64 vcc, exec, s[56:57]
	s_cbranch_vccz .LBB0_1585
	v_mov_b32_e32 v194, v141
	v_mov_b32_e32 v195, v191
	v_max_f32_e32 v134, v108, v109
	v_max3_f32 v134, v134, v110, v111
	v_max3_f32 v134, v134, v104, v105
	v_max3_f32 v134, v134, v106, v107
	v_max3_f32 v134, v134, v100, v101
	v_max3_f32 v134, v134, v102, v103
	v_max3_f32 v134, v134, v96, v97
	v_max3_f32 v134, v134, v98, v99
	v_pk_add_f32 v[158:159], v[140:141], v[134:135]
	v_cmp_le_f32_e32 vcc, v158, v159
	s_cmp_eq_u64 vcc, exec
	s_cbranch_scc1 .LBB0_1582
	v_mov_b32_e32 v134, v158
	s_nop 1
	v_permlane16_swap_b32 v158, v134
	v_max_f32_e32 v134, v134, v134
	v_max_f32_e32 v144, v158, v158
	v_max_f32_e32 v134, v144, v134
	v_mov_b32_e32 v144, v134
	s_nop 1
	v_permlane32_swap_b32 v134, v144
	v_max3_f32 v194, v141, v134, v144
	v_sub_f32_e32 v134, v141, v194
	v_exp_f32_e32 v134, v134
	v_sub_f32_e32 v144, v140, v194
	v_mul_f32_e32 v195, v191, v134
	v_add_f32_e32 v96, v96, v144
	v_add_f32_e32 v97, v97, v144
	v_add_f32_e32 v98, v98, v144
	v_add_f32_e32 v99, v99, v144
	v_add_f32_e32 v100, v100, v144
	v_add_f32_e32 v101, v101, v144
	v_add_f32_e32 v102, v102, v144
	v_add_f32_e32 v103, v103, v144
	v_add_f32_e32 v104, v104, v144
	v_add_f32_e32 v105, v105, v144
	v_add_f32_e32 v106, v106, v144
	v_add_f32_e32 v107, v107, v144
	v_add_f32_e32 v108, v108, v144
	v_add_f32_e32 v109, v109, v144
	v_add_f32_e32 v110, v110, v144
	v_add_f32_e32 v111, v111, v144
